# grid barrier: every 8th arriver of an XCD starts an early L2 write-back (3 helpers instead of 1)
# baseline (speedup 1.0000x reference)
.LBB0_236:
	s_or_b64 exec, exec, s[8:9]
	v_cvt_f32_u32_e32 v5, v3
	s_waitcnt vmcnt(0)
	v_readfirstlane_b32 s2, v4
	v_sub_u32_e32 v4, 0, v3
	v_rcp_iflag_f32_e32 v5, v5
	v_add_u32_e32 v6, s2, v2
	v_mul_f32_e32 v5, 0x4f7ffffe, v5
	v_cvt_u32_f32_e32 v5, v5
	v_mul_lo_u32 v2, v4, v5
	v_mul_hi_u32 v2, v5, v2
	v_add_u32_e32 v2, v5, v2
	v_mul_hi_u32 v2, v6, v2
	v_mul_lo_u32 v4, v2, v3
	v_sub_u32_e32 v4, v6, v4
	v_add_u32_e32 v5, 1, v2
	v_cmp_ge_u32_e32 vcc, v4, v3
	s_nop 1
	v_cndmask_b32_e32 v2, v2, v5, vcc
	v_sub_u32_e32 v5, v4, v3
	v_cndmask_b32_e32 v4, v4, v5, vcc
	v_add_u32_e32 v5, 1, v2
	v_cmp_ge_u32_e32 vcc, v4, v3
	v_add_u32_e32 v4, 1, v6
	s_nop 0
	v_cndmask_b32_e32 v2, v2, v5, vcc
	v_mul_lo_u32 v5, v3, v2
	v_add_u32_e32 v3, v5, v3
	v_cmp_ne_u32_e32 vcc, v4, v3
	s_and_saveexec_b64 s[2:3], vcc
	s_xor_b64 s[6:7], exec, s[2:3]
	s_cbranch_execz .LBB0_252
	s_waitcnt lgkmcnt(0)
	v_sub_u32_e32 v5, v3, v4
	v_and_b32_e32 v5, 7, v5
	v_cmp_ne_u32_e32 vcc, 0, v5
	s_cbranch_vccnz .Lmy_nowb_0
	buffer_wbl2 sc1

.LBB0_784:
	s_or_b64 exec, exec, s[10:11]
	v_cvt_f32_u32_e32 v5, v3
	s_waitcnt vmcnt(0)
	v_readfirstlane_b32 s8, v4
	v_sub_u32_e32 v4, 0, v3
	v_rcp_iflag_f32_e32 v5, v5
	v_add_u32_e32 v6, s8, v2
	v_mul_f32_e32 v5, 0x4f7ffffe, v5
	v_cvt_u32_f32_e32 v5, v5
	v_mul_lo_u32 v2, v4, v5
	v_mul_hi_u32 v2, v5, v2
	v_add_u32_e32 v2, v5, v2
	v_mul_hi_u32 v2, v6, v2
	v_mul_lo_u32 v4, v2, v3
	v_sub_u32_e32 v4, v6, v4
	v_add_u32_e32 v5, 1, v2
	v_cmp_ge_u32_e32 vcc, v4, v3
	s_nop 1
	v_cndmask_b32_e32 v2, v2, v5, vcc
	v_sub_u32_e32 v5, v4, v3
	v_cndmask_b32_e32 v4, v4, v5, vcc
	v_add_u32_e32 v5, 1, v2
	v_cmp_ge_u32_e32 vcc, v4, v3
	v_add_u32_e32 v4, 1, v6
	s_nop 0
	v_cndmask_b32_e32 v2, v2, v5, vcc
	v_mul_lo_u32 v5, v3, v2
	v_add_u32_e32 v3, v5, v3
	v_cmp_ne_u32_e32 vcc, v4, v3
	s_and_saveexec_b64 s[8:9], vcc
	s_xor_b64 s[8:9], exec, s[8:9]
	s_cbranch_execz .LBB0_798
	s_waitcnt lgkmcnt(0)
	v_sub_u32_e32 v5, v3, v4
	v_and_b32_e32 v5, 7, v5
	v_cmp_ne_u32_e32 vcc, 0, v5
	s_cbranch_vccnz .Lmy_nowb_2
	buffer_wbl2 sc1

.LBB0_952:
	s_or_b64 exec, exec, s[8:9]
	v_cvt_f32_u32_e32 v5, v3
	s_waitcnt vmcnt(0)
	v_readfirstlane_b32 s6, v4
	v_sub_u32_e32 v4, 0, v3
	v_rcp_iflag_f32_e32 v5, v5
	v_add_u32_e32 v6, s6, v2
	v_mul_f32_e32 v5, 0x4f7ffffe, v5
	v_cvt_u32_f32_e32 v5, v5
	v_mul_lo_u32 v2, v4, v5
	v_mul_hi_u32 v2, v5, v2
	v_add_u32_e32 v2, v5, v2
	v_mul_hi_u32 v2, v6, v2
	v_mul_lo_u32 v4, v2, v3
	v_sub_u32_e32 v4, v6, v4
	v_add_u32_e32 v5, 1, v2
	v_cmp_ge_u32_e32 vcc, v4, v3
	s_nop 1
	v_cndmask_b32_e32 v2, v2, v5, vcc
	v_sub_u32_e32 v5, v4, v3
	v_cndmask_b32_e32 v4, v4, v5, vcc
	v_add_u32_e32 v5, 1, v2
	v_cmp_ge_u32_e32 vcc, v4, v3
	v_add_u32_e32 v4, 1, v6
	s_nop 0
	v_cndmask_b32_e32 v2, v2, v5, vcc
	v_mul_lo_u32 v5, v3, v2
	v_add_u32_e32 v3, v5, v3
	v_cmp_ne_u32_e32 vcc, v4, v3
	s_and_saveexec_b64 s[6:7], vcc
	s_xor_b64 s[6:7], exec, s[6:7]
	s_cbranch_execz .LBB0_966
	s_waitcnt lgkmcnt(0)
	v_sub_u32_e32 v5, v3, v4
	v_and_b32_e32 v5, 7, v5
	v_cmp_ne_u32_e32 vcc, 0, v5
	s_cbranch_vccnz .Lmy_nowb_4
	buffer_wbl2 sc1

.LBB0_1130:
	s_or_b64 exec, exec, s[12:13]
	v_cvt_f32_u32_e32 v5, v3
	s_waitcnt vmcnt(0)
	v_readfirstlane_b32 s10, v4
	v_sub_u32_e32 v4, 0, v3
	v_rcp_iflag_f32_e32 v5, v5
	v_add_u32_e32 v6, s10, v2
	v_mul_f32_e32 v5, 0x4f7ffffe, v5
	v_cvt_u32_f32_e32 v5, v5
	v_mul_lo_u32 v2, v4, v5
	v_mul_hi_u32 v2, v5, v2
	v_add_u32_e32 v2, v5, v2
	v_mul_hi_u32 v2, v6, v2
	v_mul_lo_u32 v4, v2, v3
	v_sub_u32_e32 v4, v6, v4
	v_add_u32_e32 v5, 1, v2
	v_cmp_ge_u32_e32 vcc, v4, v3
	s_nop 1
	v_cndmask_b32_e32 v2, v2, v5, vcc
	v_sub_u32_e32 v5, v4, v3
	v_cndmask_b32_e32 v4, v4, v5, vcc
	v_add_u32_e32 v5, 1, v2
	v_cmp_ge_u32_e32 vcc, v4, v3
	v_add_u32_e32 v4, 1, v6
	s_nop 0
	v_cndmask_b32_e32 v2, v2, v5, vcc
	v_mul_lo_u32 v5, v3, v2
	v_add_u32_e32 v3, v5, v3
	v_cmp_ne_u32_e32 vcc, v4, v3
	s_and_saveexec_b64 s[10:11], vcc
	s_xor_b64 s[10:11], exec, s[10:11]
	s_cbranch_execz .LBB0_1144
	s_waitcnt lgkmcnt(0)
	v_sub_u32_e32 v5, v3, v4
	v_and_b32_e32 v5, 7, v5
	v_cmp_ne_u32_e32 vcc, 0, v5
	s_cbranch_vccnz .Lmy_nowb_6
	buffer_wbl2 sc1
